# speedup vs baseline: 1.0096x; 1.0058x over previous
.LBB0_2:
	s_or_b64 exec, exec, s[8:9]
	s_add_u32 s4, s4, s24
	s_addc_u32 s5, s5, s25
	s_barrier
	global_load_dwordx4 v[30:33], v44, s[4:5] nt
	global_load_dwordx4 v[22:25], v45, s[4:5] nt
	global_load_dwordx4 v[14:17], v47, s[4:5] nt
	s_and_saveexec_b64 s[6:7], vcc
	s_cbranch_execz .LBB0_4
	global_load_dwordx4 v[6:9], v46, s[4:5] nt
